# v37 + GEMM3 and PLE row-factor presteps: all units' loads issued together, PLE tables from one sum
# speedup vs baseline: 1.0043x; 1.0043x over previous
.LBB0_1751:
	s_andn2_b64 vcc, exec, s[2:3]
	s_cbranch_vccnz .LBB0_1837
	v_readlane_b32 s0, v255, 43
	s_waitcnt vmcnt(0)
	v_mbcnt_lo_u32_b32 v11, -1, 0
	v_mbcnt_hi_u32_b32 v11, -1, v11
	v_readlane_b32 s1, v255, 44
	v_add_u32_e32 v0, s63, v11
	s_and_b64 vcc, exec, s[0:1]
	v_readfirstlane_b32 s6, v0
	s_cbranch_vccnz .LBB0_1781
	v_lshlrev_b32_e32 v1, 4, v0
	v_add_u32_e32 v2, 0x2000, v1
	v_ashrrev_i32_e32 v3, 31, v2
	v_lshrrev_b32_e32 v3, 22, v3
	v_add_u32_e32 v3, v2, v3
	v_ashrrev_i32_e32 v8, 10, v3
	v_mul_i32_i24_e32 v3, 0x400, v8
	v_sub_u32_e32 v2, v2, v3
	v_lshrrev_b32_e32 v3, 4, v2
	v_bitop3_b32 v2, v3, v2, 32 bitop3:0x6c
	v_ashrrev_i32_e32 v3, 31, v2
	v_lshrrev_b32_e32 v3, 26, v3
	v_add_u32_e32 v3, v2, v3
	v_lshlrev_b32_e32 v4, 3, v8
	s_lshl_b32 s2, s38, 23
	v_readlane_b32 s0, v253, 52
	v_ashrrev_i32_e32 v9, 6, v3
	v_and_b32_e32 v4, -16, v4
	s_add_u32 s24, s0, s2
	v_readlane_b32 s0, v253, 53
	v_add_u32_e32 v4, v9, v4
	s_addc_u32 s25, s0, 0
	v_and_b32_e32 v5, 3, v9
	s_mov_b32 s0, 0xfffe0
	v_lshrrev_b32_e32 v6, 2, v4
	v_lshlrev_b32_e32 v7, 1, v4
	v_and_b32_e32 v3, 0xc0, v3
	v_and_or_b32 v5, v4, s0, v5
	v_and_b32_e32 v6, 4, v6
	v_and_b32_e32 v7, 24, v7
	v_sub_u32_e32 v2, v2, v3
	v_or3_b32 v5, v5, v6, v7
	v_lshlrev_b32_e32 v6, 5, v8
	v_ashrrev_i16_sdwa v2, v227, sext(v2) dst_sel:DWORD dst_unused:UNUSED_PAD src0_sel:DWORD src1_sel:BYTE_0
	v_and_b32_e32 v6, 32, v6
	v_bfe_i32 v10, v2, 0, 16
	v_add_lshl_u32 v2, v6, v10, 1
	v_lshl_add_u32 v128, v5, 12, v2
	v_lshl_add_u32 v130, v4, 12, v2
	v_bfe_i32 v2, v0, 27, 1
	v_lshrrev_b32_e32 v2, 22, v2
	v_add_u32_e32 v2, v1, v2
	v_and_b32_e32 v2, 0xfffffc00, v2
	v_sub_u32_e32 v1, v1, v2
	v_lshrrev_b32_e32 v2, 4, v1
	v_ashrrev_i32_e32 v3, 31, v0
	v_bitop3_b32 v1, v2, v1, 32 bitop3:0x6c
	v_lshrrev_b32_e32 v3, 26, v3
	v_ashrrev_i32_e32 v2, 31, v1
	v_add_u32_e32 v0, v0, v3
	v_lshrrev_b32_e32 v2, 26, v2
	v_ashrrev_i32_e32 v13, 6, v0
	v_add_u32_e32 v2, v1, v2
	v_lshlrev_b32_e32 v0, 3, v13
	v_ashrrev_i32_e32 v12, 6, v2
	v_and_b32_e32 v0, -16, v0
	s_ashr_i32 s7, s6, 6
	v_add_u32_e32 v0, v12, v0
	v_and_b32_e32 v3, 3, v12
	s_lshl_b32 s26, s7, 10
	v_and_or_b32 v3, v0, s0, v3
	v_lshrrev_b32_e32 v4, 2, v0
	v_lshlrev_b32_e32 v5, 1, v0
	v_and_b32_e32 v2, 0xc0, v2
	v_readlane_b32 s0, v253, 46
	v_and_b32_e32 v4, 4, v4
	v_and_b32_e32 v5, 24, v5
	v_sub_u32_e32 v1, v1, v2
	v_readlane_b32 s1, v253, 47
	s_add_u32 s2, s70, s0
	v_or3_b32 v3, v3, v4, v5
	v_lshlrev_b32_e32 v4, 5, v13
	v_ashrrev_i16_sdwa v1, v227, sext(v1) dst_sel:DWORD dst_unused:UNUSED_PAD src0_sel:DWORD src1_sel:BYTE_0
	s_addc_u32 s3, s71, s1
	v_readlane_b32 s0, v253, 50
	v_and_b32_e32 v4, 32, v4
	v_bfe_i32 v14, v1, 0, 16
	v_readlane_b32 s1, v253, 51
	s_add_u32 s18, s24, s0
	v_add_lshl_u32 v1, v4, v14, 1
	s_addc_u32 s19, s25, s1
	s_add_i32 s27, s26, 0
	v_lshl_add_u32 v200, v3, 12, v1
	s_add_i32 m0, s27, 0x10000
	v_lshl_add_u32 v132, v0, 12, v1
	global_load_lds_dwordx4 v200, s[18:19]
	s_add_i32 m0, s27, 0x12000
	s_add_u32 s4, s18, 0x80000
	global_load_lds_dwordx4 v128, s[18:19]
	s_addc_u32 s5, s19, 0
	s_add_i32 m0, s27, 0x14000
	s_add_i32 s28, s27, 0x2000
	global_load_lds_dwordx4 v200, s[4:5]
	s_add_i32 m0, s27, 0x16000
	v_readlane_b32 s0, v253, 54
	global_load_lds_dwordx4 v128, s[4:5]
	s_mov_b32 m0, s27
	s_add_u32 s4, s2, 0x80000
	global_load_lds_dwordx4 v132, s[2:3]
	s_mov_b32 m0, s28
	s_addc_u32 s5, s3, 0
	s_add_i32 s29, s27, 0x4000
	global_load_lds_dwordx4 v130, s[2:3]
	s_mov_b32 m0, s29
	s_add_i32 s30, s27, 0x6000
	global_load_lds_dwordx4 v132, s[4:5]
	s_mov_b32 m0, s30
	v_mov_b32_e32 v5, v201
	global_load_lds_dwordx4 v130, s[4:5]
	v_mbcnt_lo_u32_b32 v24, -1, 0
	v_mbcnt_hi_u32_b32 v24, -1, v24
	v_add_u32_e32 v24, s63, v24
	v_ashrrev_i32_e32 v25, 1, v24
	v_and_b32_e32 v26, 1, v24
	v_lshlrev_b32_e32 v28, 6, v26
	v_mov_b32_e32 v29, v201
	s_mov_b32 s9, 1
	v_readlane_b32 s12, v253, 54
	s_nop 1
	v_add_u32_e32 v56, s12, v25
	v_ashrrev_i32_e32 v57, 31, v56
	v_lshlrev_b64 v[58:59], 7, v[56:57]
	v_lshl_add_u64 v[58:59], s[66:67], 0, v[58:59]
	v_lshl_add_u64 v[58:59], v[58:59], 0, v[28:29]
	global_load_dwordx4 v[40:43], v[58:59], off
	global_load_dwordx4 v[44:47], v[58:59], off offset:16
	global_load_dwordx4 v[48:51], v[58:59], off offset:32
	global_load_dwordx4 v[52:55], v[58:59], off offset:48
	v_readlane_b32 s10, v253, 55
	v_readlane_b32 s11, v253, 56
	s_andn2_b64 vcc, exec, s[10:11]
	s_cbranch_vccnz .Lpre3_loaded
	s_mov_b32 s9, 2
	v_readlane_b32 s12, v254, 48
	s_nop 1
	v_add_u32_e32 v80, s12, v25
	v_ashrrev_i32_e32 v81, 31, v80
	v_lshlrev_b64 v[82:83], 7, v[80:81]
	v_lshl_add_u64 v[82:83], s[66:67], 0, v[82:83]
	v_lshl_add_u64 v[82:83], v[82:83], 0, v[28:29]
	global_load_dwordx4 v[64:67], v[82:83], off
	global_load_dwordx4 v[68:71], v[82:83], off offset:16
	global_load_dwordx4 v[72:75], v[82:83], off offset:32
	global_load_dwordx4 v[76:79], v[82:83], off offset:48
	v_readlane_b32 s10, v253, 57
	v_readlane_b32 s11, v253, 58
	s_andn2_b64 vcc, exec, s[10:11]
	s_cbranch_vccnz .Lpre3_loaded
	s_mov_b32 s9, 3
	v_readlane_b32 s12, v254, 49
	s_nop 1
	v_add_u32_e32 v104, s12, v25
	v_ashrrev_i32_e32 v105, 31, v104
	v_lshlrev_b64 v[106:107], 7, v[104:105]
	v_lshl_add_u64 v[106:107], s[66:67], 0, v[106:107]
	v_lshl_add_u64 v[106:107], v[106:107], 0, v[28:29]
	global_load_dwordx4 v[88:91], v[106:107], off
	global_load_dwordx4 v[92:95], v[106:107], off offset:16
	global_load_dwordx4 v[96:99], v[106:107], off offset:32
	global_load_dwordx4 v[100:103], v[106:107], off offset:48
.Lpre3_loaded:
	v_cmp_eq_u32_e32 vcc, 0, v26
	s_mov_b64 s[14:15], vcc
	v_lshl_add_u32 v25, v25, 2, 0
	s_waitcnt vmcnt(0)
	v_add_f32_e32 v40, v40, v41
	v_add_f32_e32 v42, v42, v43
	v_add_f32_e32 v40, v40, v42
	v_add_f32_e32 v44, v44, v45
	v_add_f32_e32 v46, v46, v47
	v_add_f32_e32 v44, v44, v46
	v_add_f32_e32 v48, v48, v49
	v_add_f32_e32 v50, v50, v51
	v_add_f32_e32 v48, v48, v50
	v_add_f32_e32 v52, v52, v53
	v_add_f32_e32 v54, v54, v55
	v_add_f32_e32 v52, v52, v54
	v_add_f32_e32 v40, v40, v44
	v_add_f32_e32 v48, v48, v52
	v_add_f32_e32 v40, v40, v48
	v_mov_b32_e32 v30, v201
	s_nop 1
	v_mov_b32_dpp v30, v40 quad_perm:[1,0,3,2] row_mask:0xf bank_mask:0xf
	s_mov_b64 exec, s[14:15]
	v_add_f32_e32 v31, v40, v30
	v_mov_b32_e32 v32, 0x358637bd
	v_fmamk_f32 v31, v31, 0x3a000000, v32
	s_mov_b32 s13, 0x800000
	v_mul_f32_e32 v32, 0x4b800000, v31
	v_cmp_gt_f32_e32 vcc, s13, v31
	s_nop 1
	v_cndmask_b32_e32 v31, v31, v32, vcc
	v_rsq_f32_e32 v31, v31
	s_nop 0
	v_mul_f32_e32 v32, 0x45800000, v31
	v_cndmask_b32_e32 v31, v31, v32, vcc
	v_add_u32_e32 v32, 0x25000, v25
	ds_write_b32 v32, v31
	s_mov_b64 exec, -1
	s_cmp_lt_u32 s9, 2
	s_cbranch_scc1 .Lpre3_done
	v_add_f32_e32 v64, v64, v65
	v_add_f32_e32 v66, v66, v67
	v_add_f32_e32 v64, v64, v66
	v_add_f32_e32 v68, v68, v69
	v_add_f32_e32 v70, v70, v71
	v_add_f32_e32 v68, v68, v70
	v_add_f32_e32 v72, v72, v73
	v_add_f32_e32 v74, v74, v75
	v_add_f32_e32 v72, v72, v74
	v_add_f32_e32 v76, v76, v77
	v_add_f32_e32 v78, v78, v79
	v_add_f32_e32 v76, v76, v78
	v_add_f32_e32 v64, v64, v68
	v_add_f32_e32 v72, v72, v76
	v_add_f32_e32 v64, v64, v72
	v_mov_b32_e32 v30, v201
	s_nop 1
	v_mov_b32_dpp v30, v64 quad_perm:[1,0,3,2] row_mask:0xf bank_mask:0xf
	s_mov_b64 exec, s[14:15]
	v_add_f32_e32 v31, v64, v30
	v_mov_b32_e32 v32, 0x358637bd
	v_fmamk_f32 v31, v31, 0x3a000000, v32
	s_mov_b32 s13, 0x800000
	v_mul_f32_e32 v32, 0x4b800000, v31
	v_cmp_gt_f32_e32 vcc, s13, v31
	s_nop 1
	v_cndmask_b32_e32 v31, v31, v32, vcc
	v_rsq_f32_e32 v31, v31
	s_nop 0
	v_mul_f32_e32 v32, 0x45800000, v31
	v_cndmask_b32_e32 v31, v31, v32, vcc
	v_add_u32_e32 v32, 0x25400, v25
	ds_write_b32 v32, v31
	s_mov_b64 exec, -1
	s_cmp_lt_u32 s9, 3
	s_cbranch_scc1 .Lpre3_done
	v_add_f32_e32 v88, v88, v89
	v_add_f32_e32 v90, v90, v91
	v_add_f32_e32 v88, v88, v90
	v_add_f32_e32 v92, v92, v93
	v_add_f32_e32 v94, v94, v95
	v_add_f32_e32 v92, v92, v94
	v_add_f32_e32 v96, v96, v97
	v_add_f32_e32 v98, v98, v99
	v_add_f32_e32 v96, v96, v98
	v_add_f32_e32 v100, v100, v101
	v_add_f32_e32 v102, v102, v103
	v_add_f32_e32 v100, v100, v102
	v_add_f32_e32 v88, v88, v92
	v_add_f32_e32 v96, v96, v100
	v_add_f32_e32 v88, v88, v96
	v_mov_b32_e32 v30, v201
	s_nop 1
	v_mov_b32_dpp v30, v88 quad_perm:[1,0,3,2] row_mask:0xf bank_mask:0xf
	s_mov_b64 exec, s[14:15]
	v_add_f32_e32 v31, v88, v30
	v_mov_b32_e32 v32, 0x358637bd
	v_fmamk_f32 v31, v31, 0x3a000000, v32
	s_mov_b32 s13, 0x800000
	v_mul_f32_e32 v32, 0x4b800000, v31
	v_cmp_gt_f32_e32 vcc, s13, v31
	s_nop 1
	v_cndmask_b32_e32 v31, v31, v32, vcc
	v_rsq_f32_e32 v31, v31
	s_nop 0
	v_mul_f32_e32 v32, 0x45800000, v31
	v_cndmask_b32_e32 v31, v31, v32, vcc
	v_add_u32_e32 v32, 0x25800, v25
	ds_write_b32 v32, v31
	s_mov_b64 exec, -1
.Lpre3_done:
	s_mov_b64 exec, -1
.LBB0_1762:
	s_ashr_i32 s8, s6, 8
	s_waitcnt lgkmcnt(0)
	v_mov_b32_e32 v129, v201
	v_mov_b32_e32 v133, v201
	v_mov_b32_e32 v131, v201
	s_cmp_eq_u32 s8, 1
	s_mov_b32 s48, s38
	v_lshl_add_u64 v[4:5], s[18:19], 0, v[200:201]
	v_lshl_add_u64 v[6:7], s[18:19], 0, v[128:129]
	v_lshl_add_u64 v[2:3], s[2:3], 0, v[132:133]
	v_lshl_add_u64 v[0:1], s[2:3], 0, v[130:131]
	s_cselect_b64 s[4:5], -1, 0
	s_cmp_lg_u32 s8, 1
	s_cbranch_scc1 .LBB0_1764
	s_barrier

.LBB0_2236:
	v_readlane_b32 s0, v255, 43
	v_readlane_b32 s1, v255, 44
	s_and_b64 vcc, exec, s[0:1]
	s_cbranch_vccnz .LBB0_2246
	s_waitcnt lgkmcnt(0)
	v_mbcnt_lo_u32_b32 v168, -1, 0
	v_mbcnt_hi_u32_b32 v168, -1, v168
	v_readlane_b32 s6, v254, 26
	v_readlane_b32 s7, v254, 27
	v_readlane_b32 s8, v254, 4
	v_readlane_b32 s9, v254, 5
	v_add_u32_e32 v168, s63, v168
	v_ashrrev_i32_e32 v169, 1, v168
	v_and_b32_e32 v170, 1, v168
	v_lshlrev_b32_e32 v172, 6, v170
	v_mov_b32_e32 v173, v201
	s_mov_b32 s18, 1
	v_readlane_b32 s20, v253, 54
	s_nop 1
	v_add_u32_e32 v112, s20, v169
	v_ashrrev_i32_e32 v113, 31, v112
	v_lshlrev_b64 v[114:115], 7, v[112:113]
	v_lshl_add_u64 v[114:115], s[6:7], 0, v[114:115]
	v_lshl_add_u64 v[114:115], v[114:115], 0, v[172:173]
	global_load_dwordx4 v[96:99], v[114:115], off
	global_load_dwordx4 v[100:103], v[114:115], off offset:16
	global_load_dwordx4 v[104:107], v[114:115], off offset:32
	global_load_dwordx4 v[108:111], v[114:115], off offset:48
	v_lshl_add_u64 v[112:113], v[112:113], 2, s[8:9]
	global_load_dword v116, v[112:113], off
	v_readlane_b32 s10, v253, 55
	v_readlane_b32 s11, v253, 56
	s_andn2_b64 vcc, exec, s[10:11]
	s_cbranch_vccnz .Lpre4_loaded
	s_mov_b32 s18, 2
	v_readlane_b32 s20, v254, 48
	s_nop 1
	v_add_u32_e32 v136, s20, v169
	v_ashrrev_i32_e32 v137, 31, v136
	v_lshlrev_b64 v[138:139], 7, v[136:137]
	v_lshl_add_u64 v[138:139], s[6:7], 0, v[138:139]
	v_lshl_add_u64 v[138:139], v[138:139], 0, v[172:173]
	global_load_dwordx4 v[120:123], v[138:139], off
	global_load_dwordx4 v[124:127], v[138:139], off offset:16
	global_load_dwordx4 v[128:131], v[138:139], off offset:32
	global_load_dwordx4 v[132:135], v[138:139], off offset:48
	v_lshl_add_u64 v[136:137], v[136:137], 2, s[8:9]
	global_load_dword v140, v[136:137], off
	v_readlane_b32 s10, v253, 57
	v_readlane_b32 s11, v253, 58
	s_andn2_b64 vcc, exec, s[10:11]
	s_cbranch_vccnz .Lpre4_loaded
	s_mov_b32 s18, 3
	v_readlane_b32 s20, v254, 49
	s_nop 1
	v_add_u32_e32 v160, s20, v169
	v_ashrrev_i32_e32 v161, 31, v160
	v_lshlrev_b64 v[162:163], 7, v[160:161]
	v_lshl_add_u64 v[162:163], s[6:7], 0, v[162:163]
	v_lshl_add_u64 v[162:163], v[162:163], 0, v[172:173]
	global_load_dwordx4 v[144:147], v[162:163], off
	global_load_dwordx4 v[148:151], v[162:163], off offset:16
	global_load_dwordx4 v[152:155], v[162:163], off offset:32
	global_load_dwordx4 v[156:159], v[162:163], off offset:48
	v_lshl_add_u64 v[160:161], v[160:161], 2, s[8:9]
	global_load_dword v164, v[160:161], off
.Lpre4_loaded:
	v_cmp_eq_u32_e32 vcc, 0, v170
	s_mov_b64 s[22:23], vcc
	v_lshl_add_u32 v169, v169, 2, 0
	s_waitcnt vmcnt(0)
	v_add_f32_e32 v96, v96, v97
	v_add_f32_e32 v98, v98, v99
	v_add_f32_e32 v96, v96, v98
	v_add_f32_e32 v100, v100, v101
	v_add_f32_e32 v102, v102, v103
	v_add_f32_e32 v100, v100, v102
	v_add_f32_e32 v104, v104, v105
	v_add_f32_e32 v106, v106, v107
	v_add_f32_e32 v104, v104, v106
	v_add_f32_e32 v108, v108, v109
	v_add_f32_e32 v110, v110, v111
	v_add_f32_e32 v108, v108, v110
	v_add_f32_e32 v96, v96, v100
	v_add_f32_e32 v96, v96, v104
	v_add_f32_e32 v96, v96, v108
	v_mov_b32_e32 v174, v201
	s_nop 1
	v_mov_b32_dpp v174, v96 quad_perm:[1,0,3,2] row_mask:0xf bank_mask:0xf
	s_mov_b64 exec, s[22:23]
	v_add_f32_e32 v175, v96, v174
	v_mov_b32_e32 v176, 0x358637bd
	v_fmamk_f32 v175, v175, 0x3a000000, v176
	s_mov_b32 s26, 0x800000
	v_mul_f32_e32 v176, 0x4b800000, v175
	v_cmp_gt_f32_e32 vcc, s26, v175
	s_nop 1
	v_cndmask_b32_e32 v175, v175, v176, vcc
	v_rsq_f32_e32 v175, v175
	s_nop 0
	v_mul_f32_e32 v176, 0x45800000, v175
	v_cndmask_b32_e32 v175, v175, v176, vcc
	v_mul_f32_e32 v177, 0x417e0000, v175
	v_add_u32_e32 v176, 0x25800, v169
	ds_write_b32 v176, v177
	v_div_scale_f32 v176, s[10:11], v116, v116, v175
	v_rcp_f32_e32 v177, v176
	v_div_scale_f32 v178, vcc, v175, v116, v175
	v_fma_f32 v179, -v176, v177, 1.0
	v_fmac_f32_e32 v177, v179, v177
	v_mul_f32_e32 v179, v178, v177
	v_fma_f32 v174, -v176, v179, v178
	v_fmac_f32_e32 v179, v174, v177
	v_fma_f32 v176, -v176, v179, v178
	v_div_fmas_f32 v176, v176, v177, v179
	v_div_fixup_f32 v176, v176, v116, v175
	v_add_u32_e32 v177, 0x25000, v169
	ds_write_b32 v177, v176
	s_mov_b64 exec, -1
	s_cmp_lt_u32 s18, 2
	s_cbranch_scc1 .Lpre4_done
	v_add_f32_e32 v120, v120, v121
	v_add_f32_e32 v122, v122, v123
	v_add_f32_e32 v120, v120, v122
	v_add_f32_e32 v124, v124, v125
	v_add_f32_e32 v126, v126, v127
	v_add_f32_e32 v124, v124, v126
	v_add_f32_e32 v128, v128, v129
	v_add_f32_e32 v130, v130, v131
	v_add_f32_e32 v128, v128, v130
	v_add_f32_e32 v132, v132, v133
	v_add_f32_e32 v134, v134, v135
	v_add_f32_e32 v132, v132, v134
	v_add_f32_e32 v120, v120, v124
	v_add_f32_e32 v120, v120, v128
	v_add_f32_e32 v120, v120, v132
	v_mov_b32_e32 v174, v201
	s_nop 1
	v_mov_b32_dpp v174, v120 quad_perm:[1,0,3,2] row_mask:0xf bank_mask:0xf
	s_mov_b64 exec, s[22:23]
	v_add_f32_e32 v175, v120, v174
	v_mov_b32_e32 v176, 0x358637bd
	v_fmamk_f32 v175, v175, 0x3a000000, v176
	s_mov_b32 s26, 0x800000
	v_mul_f32_e32 v176, 0x4b800000, v175
	v_cmp_gt_f32_e32 vcc, s26, v175
	s_nop 1
	v_cndmask_b32_e32 v175, v175, v176, vcc
	v_rsq_f32_e32 v175, v175
	s_nop 0
	v_mul_f32_e32 v176, 0x45800000, v175
	v_cndmask_b32_e32 v175, v175, v176, vcc
	v_mul_f32_e32 v177, 0x417e0000, v175
	v_add_u32_e32 v176, 0x25c00, v169
	ds_write_b32 v176, v177
	v_div_scale_f32 v176, s[10:11], v140, v140, v175
	v_rcp_f32_e32 v177, v176
	v_div_scale_f32 v178, vcc, v175, v140, v175
	v_fma_f32 v179, -v176, v177, 1.0
	v_fmac_f32_e32 v177, v179, v177
	v_mul_f32_e32 v179, v178, v177
	v_fma_f32 v174, -v176, v179, v178
	v_fmac_f32_e32 v179, v174, v177
	v_fma_f32 v176, -v176, v179, v178
	v_div_fmas_f32 v176, v176, v177, v179
	v_div_fixup_f32 v176, v176, v140, v175
	v_add_u32_e32 v177, 0x25400, v169
	ds_write_b32 v177, v176
	s_mov_b64 exec, -1
	s_cmp_lt_u32 s18, 3
	s_cbranch_scc1 .Lpre4_done
	v_add_f32_e32 v144, v144, v145
	v_add_f32_e32 v146, v146, v147
	v_add_f32_e32 v144, v144, v146
	v_add_f32_e32 v148, v148, v149
	v_add_f32_e32 v150, v150, v151
	v_add_f32_e32 v148, v148, v150
	v_add_f32_e32 v152, v152, v153
	v_add_f32_e32 v154, v154, v155
	v_add_f32_e32 v152, v152, v154
	v_add_f32_e32 v156, v156, v157
	v_add_f32_e32 v158, v158, v159
	v_add_f32_e32 v156, v156, v158
	v_add_f32_e32 v144, v144, v148
	v_add_f32_e32 v144, v144, v152
	v_add_f32_e32 v144, v144, v156
	v_mov_b32_e32 v174, v201
	s_nop 1
	v_mov_b32_dpp v174, v144 quad_perm:[1,0,3,2] row_mask:0xf bank_mask:0xf
	s_mov_b64 exec, s[22:23]
	v_add_f32_e32 v175, v144, v174
	v_mov_b32_e32 v176, 0x358637bd
	v_fmamk_f32 v175, v175, 0x3a000000, v176
	s_mov_b32 s26, 0x800000
	v_mul_f32_e32 v176, 0x4b800000, v175
	v_cmp_gt_f32_e32 vcc, s26, v175
	s_nop 1
	v_cndmask_b32_e32 v175, v175, v176, vcc
	v_rsq_f32_e32 v175, v175
	s_nop 0
	v_mul_f32_e32 v176, 0x45800000, v175
	v_cndmask_b32_e32 v175, v175, v176, vcc
	v_mul_f32_e32 v177, 0x417e0000, v175
	v_add_u32_e32 v176, 0x26000, v169
	ds_write_b32 v176, v177
	v_div_scale_f32 v176, s[10:11], v164, v164, v175
	v_rcp_f32_e32 v177, v176
	v_div_scale_f32 v178, vcc, v175, v164, v175
	v_fma_f32 v179, -v176, v177, 1.0
	v_fmac_f32_e32 v177, v179, v177
	v_mul_f32_e32 v179, v178, v177
	v_fma_f32 v174, -v176, v179, v178
	v_fmac_f32_e32 v179, v174, v177
	v_fma_f32 v176, -v176, v179, v178
	v_div_fmas_f32 v176, v176, v177, v179
	v_div_fixup_f32 v176, v176, v164, v175
	v_add_u32_e32 v177, 0x25800, v169
	ds_write_b32 v177, v176
	s_mov_b64 exec, -1
.Lpre4_done:
	s_mov_b64 exec, -1
.LBB0_2246:
	s_waitcnt lgkmcnt(0)
	v_readlane_b32 s0, v255, 43
	v_readlane_b32 s1, v255, 44
	s_and_b64 vcc, exec, s[0:1]
	s_waitcnt vmcnt(0) lgkmcnt(0)
	s_barrier
	s_cbranch_vccnz .LBB0_2256
.LBB0_2256:
	s_mov_b32 s39, s95
	s_lshl_b64 s[2:3], s[38:39], 22
	v_readlane_b32 s0, v254, 28
	s_add_u32 s28, s0, s2
	v_readlane_b32 s0, v254, 29
	s_addc_u32 s29, s0, s3
	s_waitcnt lgkmcnt(0)
	v_readlane_b32 s0, v255, 43
	s_waitcnt lgkmcnt(0)
	s_barrier
	v_mbcnt_lo_u32_b32 v14, -1, 0
	v_mbcnt_hi_u32_b32 v14, -1, v14
	v_readlane_b32 s1, v255, 44
	v_add_u32_e32 v0, s63, v14
	s_and_b64 vcc, exec, s[0:1]
	v_readfirstlane_b32 s2, v0
	s_cbranch_vccnz .LBB0_2258
	v_readlane_b32 s0, v254, 40
	v_readlane_b32 s1, v254, 41
	s_add_u32 s24, s28, s0
	s_addc_u32 s25, s29, s1
	v_readlane_b32 s4, v254, 38
	v_readlane_b32 s0, v254, 34
	v_readlane_b32 s5, v254, 39
	v_readlane_b32 s30, v253, 43
	s_mov_b32 s43, s0
	v_readlane_b32 s1, v254, 35
